# v73 with a branch-free rider memory block (unconditional convert, scalar selects for store target / load base, context units via negative tile counter)
# baseline (speedup 1.0000x reference)
; DI void attn_unit_a8(unsigned char* lds, const AttnArgs& a) {
;     ...
;     auto w_issue = [&](int j) __attribute__((always_inline)) { const float* src; unsigned char* dst; int ld, n0, k0; bool gu; w_decode(j, src, dst, ld, n0, k0, gu);
;         const float* p = src + (size_t)(k0 + 4 * wid) * ld + n0 + wn4;
;         wq[0] = __builtin_nontemporal_load((const f32x4*)p); wq[1] = __builtin_nontemporal_load((const f32x4*)(p + ld));
;         wq[2] = __builtin_nontemporal_load((const f32x4*)(p + (size_t)2 * ld)); wq[3] = __builtin_nontemporal_load((const f32x4*)(p + (size_t)3 * ld)); };
;     auto w_cvt = [&]() __attribute__((always_inline)) { unsigned char* t8 = lds + AT_WT + wn4 * WPITCH + 4 * wid;
; #pragma unroll
;         for (int j = 0; j < 4; ++j) *(unsigned*)(t8 + j * WPITCH) = pk4_fp8_mul64(wq[0][j], wq[1][j], wq[2][j], wq[3][j]); };
;     const int wcol = tid >> 1, whalf = tid & 1;
;     const unsigned wper_gu = (unsigned)((wcol >> 7) * 256 + (wcol & 96) + invperm32(wcol & 31)) * 1024u + 16u * whalf;
;     const unsigned wper_dn = (unsigned)fwd_lane16(wcol) * 1024u + 16u * whalf;
;     auto w_store = [&](int j) __attribute__((always_inline)) { const float* src; unsigned char* dst; int ld, n0, k0; bool gu; w_decode(j, src, dst, ld, n0, k0, gu);
;         const int nb = n0 >> 8; const unsigned uni = (unsigned)(gu ? (nb & 3) * 512 + (nb >> 2) * 128 : nb * 256) * 1024u + (unsigned)k0;
;         const unsigned off = (gu ? wper_gu : wper_dn) + uni;
;         const unsigned* t = (const unsigned*)(lds + AT_WT + wcol * WPITCH + 16 * whalf);
;         *(u32x4*)(dst + off) = (u32x4){t[0], t[1], t[2], t[3]}; };
; DI void attn_unit_d8(unsigned char* lds, const AttnArgs& a) {
;     ...
;     for (int t = a.t0; t < a.t1; t += 2) {
;         const int s1 = sb + 1 >= 5 ? sb - 4 : sb + 1, s2 = sb + 2 >= 5 ? sb - 3 : sb + 2, s3 = sb + 3 >= 5 ? sb - 2 : sb + 3, s4 = sb + 4 >= 5 ? sb - 1 : sb + 4;
;         { const int ta = t + 3, tb = t + 4; gload(ta < a.t1 ? ta : a.t1 - 1, kreg0, vreg0); gload(tb < a.t1 ? tb : a.t1 - 1, kreg1, vreg1); }
;         tile(lds + sb * D8_SLOT, lds + s1 * D8_SLOT, PaX, PbX, vX0, vX1, PaY, PbY, vY0, vY1);
;         tile(lds + s1 * D8_SLOT, lds + s2 * D8_SLOT, PaY, PbY, vY0, vY1, PaX, PbX, vX0, vX1);
;         lstore(s3, kreg0, vreg0); lstore(s4, kreg1, vreg1);
;         __syncthreads();
;         sb = s2;
;     }
.Lmy_rd0_nodec:
	s_waitcnt vmcnt(4)
	v_cvt_scalef32_pk_fp8_f32 v236, v236, v240, s62
	v_cvt_scalef32_pk_fp8_f32 v237, v237, v241, s62
	v_cvt_scalef32_pk_fp8_f32 v238, v238, v242, s62
	v_cvt_scalef32_pk_fp8_f32 v239, v239, v243, s62
	v_cvt_scalef32_pk_fp8_f32 v236, v244, v248, s62 op_sel:[0,0,0,1]
	v_cvt_scalef32_pk_fp8_f32 v237, v245, v249, s62 op_sel:[0,0,0,1]
	v_cvt_scalef32_pk_fp8_f32 v238, v246, v250, s62 op_sel:[0,0,0,1]
	v_cvt_scalef32_pk_fp8_f32 v239, v247, v251, s62 op_sel:[0,0,0,1]
	s_add_i32 s72, s61, -2
	ds_write_b32 v252, v236
	ds_write_b32 v252, v237 offset:36
	ds_write_b32 v252, v238 offset:72
	ds_write_b32 v252, v239 offset:108
	ds_read2_b32 v[244:245], v253 offset1:1
	ds_read2_b32 v[246:247], v253 offset0:2 offset1:3
	s_cmp_lt_u32 s72, 24
	s_cselect_b32 s73, s65, 0x1c094000
	s_bitcmp1_b32 s73, 0
	s_cselect_b64 vcc, -1, 0
	s_andn2_b32 s73, s73, 1
	s_add_u32 s82, s70, s73
	s_addc_u32 s83, s71, 0
	v_cndmask_b32_e32 v248, v254, v255, vcc
	s_cmp_lt_u32 s61, 24
	s_cselect_b32 s84, s84, s70
	s_cselect_b32 s85, s85, s71
	s_cselect_b32 s80, s80, 0
	s_waitcnt lgkmcnt(0)
	global_store_dwordx4 v248, v[244:247], s[82:83]
	global_load_dwordx4 v[236:239], v235, s[84:85] nt
	s_add_u32 s84, s84, s80
	s_addc_u32 s85, s85, 0
	global_load_dwordx4 v[240:243], v235, s[84:85] nt
	s_add_u32 s84, s84, s80
	s_addc_u32 s85, s85, 0
	global_load_dwordx4 v[244:247], v235, s[84:85] nt
	s_add_u32 s84, s84, s80
	s_addc_u32 s85, s85, 0
	global_load_dwordx4 v[248:251], v235, s[84:85] nt
	s_mov_b32 s65, s58
	s_mov_b32 s58, s79
	s_mul_i32 s72, s80, 29
	s_add_u32 s84, s84, s72
	s_addc_u32 s85, s85, 0
	s_add_i32 s79, s79, 32
	v_xor_b32_e32 v252, 0x4000, v252
	v_xor_b32_e32 v253, 0x4000, v253
	s_add_i32 s61, s61, 1
	s_add_i32 s18, s46, 2
	s_cmpk_lt_u32 s46, 0x42
	s_mov_b32 s46, s18
	s_waitcnt vmcnt(6)
	ds_write_b64 v224, v[192:193]
	v_mfma_f32_32x32x64_f8f6f4 v[66:81], v[98:105], v[122:129], 0
	v_add_u32_e32 v98, 0x1400, v225
	v_add_u32_e32 v99, 0x1400, v107
	ds_write2_b32 v98, v202, v203 offset1:8
	s_waitcnt vmcnt(5)
	ds_write_b64 v106, v[194:195]
	ds_write2_b32 v99, v204, v205 offset1:8
	s_waitcnt lgkmcnt(0)
	s_barrier
	s_cbranch_scc1 .LBB0_663
	s_lshl_b64 s[14:15], s[14:15], 10
	s_add_u32 s6, s8, s14
	s_addc_u32 s15, s9, s15
	s_add_u32 s14, s6, s43
	v_mfma_f32_32x32x64_f8f6f4 v[50:65], v[154:161], v[138:145], v[50:65]
	s_addc_u32 s15, s15, 0
	v_mfma_f32_32x32x64_f8f6f4 v[2:17], v[154:161], v[130:137], v[2:17]
	v_mfma_f32_32x32x64_f8f6f4 v[34:49], v[146:153], v[138:145], v[34:49]
	v_mfma_f32_32x32x64_f8f6f4 v[18:33], v[146:153], v[130:137], v[18:33]
	s_setprio 0
	v_add_f32_e32 v66, v186, v187
	v_add_f32_e32 v66, v184, v66
	v_add_f32_e32 v66, v185, v66
	ds_bpermute_b32 v67, v1, v66
	v_add_f32_e32 v68, v190, v191
	v_add_f32_e32 v68, v188, v68
	v_add_f32_e32 v68, v189, v68
	ds_bpermute_b32 v69, v1, v68
	s_waitcnt lgkmcnt(1)
	v_add_f32_e32 v66, v66, v67
	v_div_scale_f32 v67, s[16:17], v66, v66, s36
	v_rcp_f32_e32 v70, v67
	s_waitcnt lgkmcnt(0)
	v_add_f32_e32 v68, v68, v69
	v_lshlrev_b32_e32 v178, 2, v214
	s_add_i32 s42, s42, s64
	v_fma_f32 v69, -v67, v70, 1.0
	v_fmac_f32_e32 v70, v69, v70
	v_div_scale_f32 v69, vcc, s36, v66, s36
	v_mul_f32_e32 v71, v69, v70
	v_fma_f32 v72, -v67, v71, v69
	v_fmac_f32_e32 v71, v72, v70
	v_fma_f32 v67, -v67, v71, v69
	v_div_scale_f32 v69, s[16:17], v68, v68, v211
	v_rcp_f32_e32 v72, v69
	v_div_fmas_f32 v67, v67, v70, v71
	v_div_fixup_f32 v66, v67, v66, s36
	s_cmpk_gt_i32 s42, 0x21f
	v_fma_f32 v67, -v69, v72, 1.0
	v_fmac_f32_e32 v72, v67, v72
	v_div_scale_f32 v67, vcc, v211, v68, v211
	v_mul_f32_e32 v70, v67, v72
	v_fma_f32 v71, -v69, v70, v67
	v_fmac_f32_e32 v70, v71, v72
	v_fma_f32 v67, -v69, v70, v67
	v_div_fmas_f32 v67, v67, v72, v70
	v_div_fixup_f32 v68, v67, v68, v211
	v_mul_f32_e32 v2, v2, v68
	v_fma_f32 v50, v50, v66, -v2
	v_mul_f32_e32 v2, v3, v68
	v_fma_f32 v51, v51, v66, -v2
	v_mul_f32_e32 v67, v51, v51
	v_mul_f32_e32 v2, v4, v68
	v_fmac_f32_e32 v67, v50, v50
	v_fma_f32 v52, v52, v66, -v2
	v_mul_f32_e32 v2, v5, v68
	v_fmac_f32_e32 v67, v52, v52
	v_fma_f32 v53, v53, v66, -v2
	v_mul_f32_e32 v2, v6, v68
	v_fmac_f32_e32 v67, v53, v53
	v_fma_f32 v54, v54, v66, -v2
	v_mul_f32_e32 v2, v7, v68
	v_fmac_f32_e32 v67, v54, v54
	v_fma_f32 v55, v55, v66, -v2
	v_mul_f32_e32 v2, v8, v68
	v_fmac_f32_e32 v67, v55, v55
	v_fma_f32 v56, v56, v66, -v2
	v_mul_f32_e32 v2, v9, v68
	v_fmac_f32_e32 v67, v56, v56
	v_fma_f32 v57, v57, v66, -v2
	v_mul_f32_e32 v2, v10, v68
	v_fmac_f32_e32 v67, v57, v57
	v_fma_f32 v58, v58, v66, -v2
	v_mul_f32_e32 v2, v11, v68
	v_fmac_f32_e32 v67, v58, v58
	v_fma_f32 v59, v59, v66, -v2
	v_mul_f32_e32 v2, v12, v68
	v_fmac_f32_e32 v67, v59, v59
	v_fma_f32 v60, v60, v66, -v2
	v_mul_f32_e32 v2, v13, v68
	v_fmac_f32_e32 v67, v60, v60
	v_fma_f32 v61, v61, v66, -v2
	v_mul_f32_e32 v14, v14, v68
	v_fmac_f32_e32 v67, v61, v61
	v_fma_f32 v62, v62, v66, -v14
	v_mul_f32_e32 v14, v15, v68
	v_fmac_f32_e32 v67, v62, v62
	v_fma_f32 v63, v63, v66, -v14
	v_mul_f32_e32 v14, v16, v68
	v_lshlrev_b32_e32 v69, 4, v214
	v_fmac_f32_e32 v67, v63, v63
	v_fma_f32 v64, v64, v66, -v14
	v_mul_f32_e32 v14, v17, v68
	global_load_dwordx4 v[2:5], v69, s[10:11] offset:224
	global_load_dwordx4 v[6:9], v69, s[10:11] offset:32
	global_load_dwordx4 v[10:13], v69, s[10:11]
	v_fmac_f32_e32 v67, v64, v64
	v_fma_f32 v65, v65, v66, -v14
	v_mul_f32_e32 v14, v18, v68
	v_fmac_f32_e32 v67, v65, v65
	v_fma_f32 v70, v34, v66, -v14
	v_mul_f32_e32 v14, v19, v68
	v_fmac_f32_e32 v67, v70, v70
	v_fma_f32 v71, v35, v66, -v14
	v_mul_f32_e32 v14, v20, v68
	v_fmac_f32_e32 v67, v71, v71
	v_fma_f32 v72, v36, v66, -v14
	v_mul_f32_e32 v14, v21, v68
	v_fmac_f32_e32 v67, v72, v72
; DI unsigned pk4_fp8(float a, float b, float c, float d) { int r = 0; r = __builtin_amdgcn_cvt_pk_fp8_f32(a, b, r, false); r = __builtin_amdgcn_cvt_pk_fp8_f32(c, d, r, true); return (unsigned)r; }
; DI float clamp448(float x) { return __builtin_amdgcn_fmed3f(x, -448.0f, 448.0f); }
; DI void attn_unit_d8(unsigned char* lds, const AttnArgs& a) {
;     ...
;     const float r0 = 16.0f / lt0, r1 = 16.0f * a.lam / lt1;
;     float ss = 0.f;
; #pragma unroll
;     for (int d = 0; d < 2; ++d)
; #pragma unroll
;         for (int i = 0; i < 16; ++i) { const float v = o0[d][i] * r0 - o1[d][i] * r1; o0[d][i] = v; ss += v * v; }
;     ss += __shfl_xor(ss, 32);
;     const float rinv = rsqrtf(ss * (1.0f / 64.0f) + EPS) * a.oscale * CAT_SCALE;
;     f32x4 ggv[2][4];
; #pragma unroll
;     for (int d = 0; d < 2; ++d)
; #pragma unroll
;         for (int g = 0; g < 4; ++g) ggv[d][g] = *(const f32x4*)(a.subg + 32 * d + 8 * g + 4 * h);
;     asm volatile("" : "+v"(ggv[0][0]), "+v"(ggv[1][3]));
; #pragma unroll
;     for (int d = 0; d < 2; ++d)
; #pragma unroll
;         for (int g = 0; g < 4; ++g) { const f32x4 gg = ggv[d][g];
;             *(unsigned*)(op + 32 * d + 8 * g) = pk4_fp8(clamp448(o0[d][4 * g] * rinv * gg[0]), clamp448(o0[d][4 * g + 1] * rinv * gg[1]), clamp448(o0[d][4 * g + 2] * rinv * gg[2]), clamp448(o0[d][4 * g + 3] * rinv * gg[3])); }
	v_fma_f32 v73, v37, v66, -v14
	v_mul_f32_e32 v14, v22, v68
	v_fmac_f32_e32 v67, v73, v73
	v_fma_f32 v74, v38, v66, -v14
	v_mul_f32_e32 v14, v23, v68
	v_fmac_f32_e32 v67, v74, v74
	v_fma_f32 v75, v39, v66, -v14
	v_fmac_f32_e32 v67, v75, v75
	v_pk_mul_f32 v[14:15], v[24:25], v[68:69] op_sel_hi:[1,0]
	v_pk_mul_f32 v[22:23], v[32:33], v[68:69] op_sel_hi:[1,0]
	v_pk_fma_f32 v[34:35], v[40:41], v[66:67], v[14:15] op_sel_hi:[1,0,1] neg_lo:[0,0,1] neg_hi:[0,0,1]
	s_nop 0
	v_pk_mul_f32 v[14:15], v[34:35], v[34:35]
	s_nop 0
	v_add_f32_e32 v14, v14, v67
	v_add_f32_e32 v20, v15, v14
	v_pk_mul_f32 v[14:15], v[26:27], v[68:69] op_sel_hi:[1,0]
	s_nop 0
	v_pk_fma_f32 v[36:37], v[42:43], v[66:67], v[14:15] op_sel_hi:[1,0,1] neg_lo:[0,0,1] neg_hi:[0,0,1]
	global_load_dwordx4 v[14:17], v69, s[10:11] offset:64
	v_pk_mul_f32 v[18:19], v[36:37], v[36:37]
	v_pk_fma_f32 v[42:43], v[48:49], v[66:67], v[22:23] op_sel_hi:[1,0,1] neg_lo:[0,0,1] neg_hi:[0,0,1]
	v_add_f32_e32 v18, v18, v20
	v_add_f32_e32 v20, v19, v18
	v_pk_mul_f32 v[18:19], v[28:29], v[68:69] op_sel_hi:[1,0]
	v_pk_mul_f32 v[22:23], v[42:43], v[42:43]
	v_pk_fma_f32 v[38:39], v[44:45], v[66:67], v[18:19] op_sel_hi:[1,0,1] neg_lo:[0,0,1] neg_hi:[0,0,1]
	s_nop 0
	v_pk_mul_f32 v[18:19], v[38:39], v[38:39]
	s_nop 0
	v_add_f32_e32 v18, v18, v20
	v_add_f32_e32 v20, v19, v18
	v_pk_mul_f32 v[18:19], v[30:31], v[68:69] op_sel_hi:[1,0]
	s_nop 0
	v_pk_fma_f32 v[40:41], v[46:47], v[66:67], v[18:19] op_sel_hi:[1,0,1] neg_lo:[0,0,1] neg_hi:[0,0,1]
	s_nop 0
	v_pk_mul_f32 v[18:19], v[40:41], v[40:41]
	s_nop 0
	v_add_f32_e32 v18, v18, v20
	v_add_f32_e32 v24, v19, v18
	v_add_f32_e32 v22, v22, v24
	v_add_f32_e32 v26, v23, v22
	ds_bpermute_b32 v27, v1, v26
	global_load_dwordx4 v[18:21], v69, s[10:11] offset:96
	global_load_dwordx4 v[22:25], v69, s[10:11] offset:192
	s_waitcnt lgkmcnt(0)
	v_add_f32_e32 v26, v26, v27
	v_fmamk_f32 v26, v26, 0x3c800000, v212
	v_mul_f32_e32 v27, 0x4b800000, v26
	v_cmp_gt_f32_e32 vcc, s39, v26
	s_nop 1
	v_cndmask_b32_e32 v30, v26, v27, vcc
	global_load_dwordx4 v[26:29], v69, s[10:11] offset:128
	v_rsq_f32_e32 v32, v30
	v_lshlrev_b64 v[30:31], 10, v[180:181]
	v_lshl_add_u64 v[44:45], s[14:15], 0, v[30:31]
	v_lshl_add_u64 v[44:45], v[44:45], 0, v[178:179]
	v_mul_f32_e32 v30, 0x45800000, v32
	v_cndmask_b32_e32 v30, v32, v30, vcc
	v_mul_f32_e32 v48, 0x3f4ccccd, v30
	global_load_dwordx4 v[30:33], v69, s[10:11] offset:160
	v_mul_f32_e32 v48, 0x41800000, v48
	s_waitcnt vmcnt(5)
	v_mul_f32_e32 v49, v50, v48
	v_mul_f32_e32 v10, v10, v49
	v_mul_f32_e32 v49, v51, v48
	v_mul_f32_e32 v11, v11, v49
	v_mul_f32_e32 v49, v52, v48
	v_med3_f32 v10, v10, s40, v213
	v_med3_f32 v11, v11, s40, v213
	v_mul_f32_e32 v12, v12, v49
	s_nop 0
	v_cvt_pk_fp8_f32 v49, v10, v11
	v_mul_f32_e32 v10, v53, v48
	v_mul_f32_e32 v10, v13, v10
	v_med3_f32 v12, v12, s40, v213
	v_med3_f32 v10, v10, s40, v213
	v_cvt_pk_fp8_f32 v49, v12, v10 op_sel:[0,0,1]
	v_mul_f32_e32 v10, v54, v48
	v_mul_f32_e32 v6, v6, v10
	v_mul_f32_e32 v10, v55, v48
	v_mul_f32_e32 v7, v7, v10
	v_mul_f32_e32 v10, v56, v48
	v_med3_f32 v6, v6, s40, v213
	v_med3_f32 v7, v7, s40, v213
	v_mul_f32_e32 v8, v8, v10
	s_nop 0
	v_cvt_pk_fp8_f32 v10, v6, v7
	v_mul_f32_e32 v6, v57, v48
	v_mul_f32_e32 v6, v9, v6
	v_med3_f32 v8, v8, s40, v213
	v_med3_f32 v6, v6, s40, v213
	v_cvt_pk_fp8_f32 v10, v8, v6 op_sel:[0,0,1]
	v_add_co_u32_e32 v6, vcc, s41, v44
	v_lshl_add_u64 v[46:47], v[44:45], 0, s[12:13]
	s_nop 0
	v_addc_co_u32_e32 v7, vcc, 0, v45, vcc
	global_store_dword v[6:7], v49, off offset:768
	global_store_dword v[46:47], v10, off offset:8
	v_mul_f32_e32 v6, v58, v48
	v_mul_f32_e32 v7, v59, v48
	s_waitcnt vmcnt(6)
	v_mul_f32_e32 v6, v14, v6
	v_mul_f32_e32 v7, v15, v7
	v_med3_f32 v6, v6, s40, v213
	v_med3_f32 v7, v7, s40, v213
	s_nop 0
	v_cvt_pk_fp8_f32 v9, v6, v7
	v_mul_f32_e32 v8, v60, v48
	v_mul_f32_e32 v6, v61, v48
	v_mul_f32_e32 v8, v16, v8
	v_mul_f32_e32 v6, v17, v6
	v_med3_f32 v8, v8, s40, v213
	v_med3_f32 v6, v6, s40, v213
	v_cvt_pk_fp8_f32 v9, v8, v6 op_sel:[0,0,1]
	v_mul_f32_e32 v6, v62, v48
	v_mul_f32_e32 v7, v63, v48
	s_nop 0
	v_mul_f32_e32 v8, v64, v48
	s_nop 0
	s_waitcnt vmcnt(5)
	v_mul_f32_e32 v6, v18, v6
	v_mul_f32_e32 v7, v19, v7
	v_med3_f32 v6, v6, s40, v213
	v_med3_f32 v7, v7, s40, v213
	v_cvt_pk_fp8_f32 v10, v6, v7
	v_mul_f32_e32 v6, v65, v48
	v_mul_f32_e32 v8, v20, v8
	v_mul_f32_e32 v6, v21, v6
	v_med3_f32 v8, v8, s40, v213
	v_med3_f32 v6, v6, s40, v213
	v_cvt_pk_fp8_f32 v10, v8, v6 op_sel:[0,0,1]
	v_mul_f32_e32 v6, v70, v48
	v_mul_f32_e32 v7, v71, v48
	s_waitcnt vmcnt(3)
	v_mul_f32_e32 v6, v26, v6
	v_mul_f32_e32 v7, v27, v7
	v_med3_f32 v6, v6, s40, v213
	v_med3_f32 v7, v7, s40, v213
	v_cvt_pk_fp8_f32 v11, v6, v7
	v_mul_f32_e32 v8, v72, v48
	v_mul_f32_e32 v6, v73, v48
	v_mul_f32_e32 v8, v28, v8
	v_mul_f32_e32 v6, v29, v6
	v_med3_f32 v8, v8, s40, v213
	v_med3_f32 v6, v6, s40, v213
	v_cvt_pk_fp8_f32 v11, v8, v6 op_sel:[0,0,1]
	v_mul_f32_e32 v6, v74, v48
	v_mul_f32_e32 v7, v75, v48
	s_waitcnt vmcnt(2)
	v_mul_f32_e32 v6, v30, v6
	v_mul_f32_e32 v7, v31, v7
	v_med3_f32 v6, v6, s40, v213
	v_med3_f32 v7, v7, s40, v213
	s_nop 0
	v_cvt_pk_fp8_f32 v12, v6, v7
	v_mul_f32_e32 v8, v34, v48
	v_mul_f32_e32 v6, v35, v48
	v_mul_f32_e32 v8, v32, v8
	v_mul_f32_e32 v6, v33, v6
	v_med3_f32 v8, v8, s40, v213
	v_med3_f32 v6, v6, s40, v213
	v_cvt_pk_fp8_f32 v12, v8, v6 op_sel:[0,0,1]
	v_mul_f32_e32 v6, v36, v48
	v_mul_f32_e32 v7, v37, v48
	v_mul_f32_e32 v6, v22, v6
	v_mul_f32_e32 v7, v23, v7
	global_store_dword v[46:47], v9, off offset:16
	global_store_dword v[46:47], v10, off offset:24
	global_store_dword v[46:47], v11, off offset:32
	global_store_dword v[46:47], v12, off offset:40
	v_med3_f32 v6, v6, s40, v213
	v_med3_f32 v7, v7, s40, v213
	s_nop 0
	v_cvt_pk_fp8_f32 v9, v6, v7
	v_mul_f32_e32 v8, v38, v48
	v_mul_f32_e32 v6, v39, v48
	v_mul_f32_e32 v8, v24, v8
	v_mul_f32_e32 v6, v25, v6
	v_med3_f32 v8, v8, s40, v213
	v_med3_f32 v6, v6, s40, v213
	v_cvt_pk_fp8_f32 v9, v8, v6 op_sel:[0,0,1]
	v_mul_f32_e32 v6, v40, v48
	v_mul_f32_e32 v2, v2, v6
	v_mul_f32_e32 v6, v41, v48
	v_mul_f32_e32 v3, v3, v6
	v_mul_f32_e32 v6, v42, v48
	v_med3_f32 v2, v2, s40, v213
	v_med3_f32 v3, v3, s40, v213
	v_mul_f32_e32 v4, v4, v6
	s_nop 0
	v_cvt_pk_fp8_f32 v6, v2, v3
	v_mul_f32_e32 v2, v43, v48
	v_mul_f32_e32 v2, v5, v2
	v_med3_f32 v4, v4, s40, v213
	v_med3_f32 v2, v2, s40, v213
	v_cvt_pk_fp8_f32 v6, v4, v2 op_sel:[0,0,1]
	global_store_dword v[46:47], v9, off offset:48
	global_store_dword v[46:47], v6, off offset:56
	s_cbranch_scc0 .LBB0_656

; DI void attn_unit_a8(unsigned char* lds, const AttnArgs& a) {
;     ...
;     auto w_issue = [&](int j) __attribute__((always_inline)) { const float* src; unsigned char* dst; int ld, n0, k0; bool gu; w_decode(j, src, dst, ld, n0, k0, gu);
;         const float* p = src + (size_t)(k0 + 4 * wid) * ld + n0 + wn4;
;         wq[0] = __builtin_nontemporal_load((const f32x4*)p); wq[1] = __builtin_nontemporal_load((const f32x4*)(p + ld));
;         wq[2] = __builtin_nontemporal_load((const f32x4*)(p + (size_t)2 * ld)); wq[3] = __builtin_nontemporal_load((const f32x4*)(p + (size_t)3 * ld)); };
;     auto w_cvt = [&]() __attribute__((always_inline)) { unsigned char* t8 = lds + AT_WT + wn4 * WPITCH + 4 * wid;
; #pragma unroll
;         for (int j = 0; j < 4; ++j) *(unsigned*)(t8 + j * WPITCH) = pk4_fp8_mul64(wq[0][j], wq[1][j], wq[2][j], wq[3][j]); };
;     const int wcol = tid >> 1, whalf = tid & 1;
;     const unsigned wper_gu = (unsigned)((wcol >> 7) * 256 + (wcol & 96) + invperm32(wcol & 31)) * 1024u + 16u * whalf;
;     const unsigned wper_dn = (unsigned)fwd_lane16(wcol) * 1024u + 16u * whalf;
;     auto w_store = [&](int j) __attribute__((always_inline)) { const float* src; unsigned char* dst; int ld, n0, k0; bool gu; w_decode(j, src, dst, ld, n0, k0, gu);
;         const int nb = n0 >> 8; const unsigned uni = (unsigned)(gu ? (nb & 3) * 512 + (nb >> 2) * 128 : nb * 256) * 1024u + (unsigned)k0;
;         const unsigned off = (gu ? wper_gu : wper_dn) + uni;
;         const unsigned* t = (const unsigned*)(lds + AT_WT + wcol * WPITCH + 16 * whalf);
;         *(u32x4*)(dst + off) = (u32x4){t[0], t[1], t[2], t[3]}; };
; DI void attn_unit_d8(unsigned char* lds, const AttnArgs& a) {
;     ...
;     for (int t = a.t0; t < a.t1; t += 2) {
;         const int s1 = sb + 1 >= 5 ? sb - 4 : sb + 1, s2 = sb + 2 >= 5 ? sb - 3 : sb + 2, s3 = sb + 3 >= 5 ? sb - 2 : sb + 3, s4 = sb + 4 >= 5 ? sb - 1 : sb + 4;
;         { const int ta = t + 3, tb = t + 4; gload(ta < a.t1 ? ta : a.t1 - 1, kreg0, vreg0); gload(tb < a.t1 ? tb : a.t1 - 1, kreg1, vreg1); }
;         tile(lds + sb * D8_SLOT, lds + s1 * D8_SLOT, PaX, PbX, vX0, vX1, PaY, PbY, vY0, vY1);
;         tile(lds + s1 * D8_SLOT, lds + s2 * D8_SLOT, PaY, PbY, vY0, vY1, PaX, PbX, vX0, vX1);
;         lstore(s3, kreg0, vreg0); lstore(s4, kreg1, vreg1);
;         __syncthreads();
;         sb = s2;
;     }
.Lmy_rd1_nodec:
	s_waitcnt vmcnt(4)
	v_cvt_scalef32_pk_fp8_f32 v236, v236, v240, s62
	v_cvt_scalef32_pk_fp8_f32 v237, v237, v241, s62
	v_cvt_scalef32_pk_fp8_f32 v238, v238, v242, s62
	v_cvt_scalef32_pk_fp8_f32 v239, v239, v243, s62
	v_cvt_scalef32_pk_fp8_f32 v236, v244, v248, s62 op_sel:[0,0,0,1]
	v_cvt_scalef32_pk_fp8_f32 v237, v245, v249, s62 op_sel:[0,0,0,1]
	v_cvt_scalef32_pk_fp8_f32 v238, v246, v250, s62 op_sel:[0,0,0,1]
	v_cvt_scalef32_pk_fp8_f32 v239, v247, v251, s62 op_sel:[0,0,0,1]
	s_add_i32 s72, s61, -2
	ds_write_b32 v252, v236
	ds_write_b32 v252, v237 offset:36
	ds_write_b32 v252, v238 offset:72
	ds_write_b32 v252, v239 offset:108
	ds_read2_b32 v[244:245], v253 offset1:1
	ds_read2_b32 v[246:247], v253 offset0:2 offset1:3
	s_cmp_lt_u32 s72, 24
	s_cselect_b32 s73, s65, 0x1c094000
	s_bitcmp1_b32 s73, 0
	s_cselect_b64 vcc, -1, 0
	s_andn2_b32 s73, s73, 1
	s_add_u32 s82, s70, s73
	s_addc_u32 s83, s71, 0
	v_cndmask_b32_e32 v248, v254, v255, vcc
	s_cmp_lt_u32 s61, 24
	s_cselect_b32 s84, s84, s70
	s_cselect_b32 s85, s85, s71
	s_cselect_b32 s80, s80, 0
	s_waitcnt lgkmcnt(0)
	global_store_dwordx4 v248, v[244:247], s[82:83]
	global_load_dwordx4 v[236:239], v235, s[84:85] nt
	s_add_u32 s84, s84, s80
	s_addc_u32 s85, s85, 0
	global_load_dwordx4 v[240:243], v235, s[84:85] nt
	s_add_u32 s84, s84, s80
	s_addc_u32 s85, s85, 0
	global_load_dwordx4 v[244:247], v235, s[84:85] nt
	s_add_u32 s84, s84, s80
	s_addc_u32 s85, s85, 0
	global_load_dwordx4 v[248:251], v235, s[84:85] nt
	s_mov_b32 s65, s64
	s_mov_b32 s64, s79
	s_mul_i32 s72, s80, 29
	s_add_u32 s84, s84, s72
	s_addc_u32 s85, s85, 0
	s_add_i32 s79, s79, 32
	v_xor_b32_e32 v252, 0x4000, v252
	v_xor_b32_e32 v253, 0x4000, v253
	s_add_i32 s61, s61, 1
	s_cmpk_lt_u32 s22, 0x42
	s_waitcnt vmcnt(6)
	ds_write_b64 v224, v[194:195]
	v_mfma_f32_32x32x64_f8f6f4 v[66:81], v[98:105], v[122:129], 0
	v_add_u32_e32 v98, s51, v218
	v_add_u32_e32 v99, 0x1400, v106
	v_add_u32_e32 v98, 0x1400, v98
	ds_write2_b32 v99, v204, v205 offset1:8
	s_waitcnt vmcnt(5)
	ds_write_b64 v107, v[196:197]
	ds_write2_b32 v98, v206, v207 offset1:8
	s_waitcnt lgkmcnt(0)
	s_barrier
	s_cbranch_scc1 .LBB0_1888
	s_lshl_b64 s[16:17], s[16:17], 10
	s_add_u32 s8, s10, s16
	s_addc_u32 s17, s11, s17
	s_add_u32 s16, s8, s47
	v_mfma_f32_32x32x64_f8f6f4 v[50:65], v[154:161], v[138:145], v[50:65]
	s_addc_u32 s17, s17, 0
	v_mfma_f32_32x32x64_f8f6f4 v[2:17], v[154:161], v[130:137], v[2:17]
	v_mfma_f32_32x32x64_f8f6f4 v[34:49], v[146:153], v[138:145], v[34:49]
	v_mfma_f32_32x32x64_f8f6f4 v[18:33], v[146:153], v[130:137], v[18:33]
	s_setprio 0
	v_add_f32_e32 v66, v188, v189
	v_add_f32_e32 v66, v186, v66
	v_add_f32_e32 v66, v187, v66
	ds_bpermute_b32 v67, v1, v66
	v_add_f32_e32 v68, v192, v193
	v_add_f32_e32 v68, v190, v68
	v_add_f32_e32 v68, v191, v68
	ds_bpermute_b32 v69, v1, v68
	s_waitcnt lgkmcnt(1)
	v_add_f32_e32 v66, v66, v67
	v_div_scale_f32 v67, s[18:19], v66, v66, s36
	v_rcp_f32_e32 v70, v67
	s_waitcnt lgkmcnt(0)
	v_add_f32_e32 v68, v68, v69
	v_lshlrev_b32_e32 v178, 2, v217
	s_add_i32 s46, s46, s60
	v_fma_f32 v69, -v67, v70, 1.0
	v_fmac_f32_e32 v70, v69, v70
	v_div_scale_f32 v69, vcc, s36, v66, s36
	v_mul_f32_e32 v71, v69, v70
	v_fma_f32 v72, -v67, v71, v69
	v_fmac_f32_e32 v71, v72, v70
	v_fma_f32 v67, -v67, v71, v69
	v_div_scale_f32 v69, s[18:19], v68, v68, v214
	v_rcp_f32_e32 v72, v69
	v_div_fmas_f32 v67, v67, v70, v71
	v_div_fixup_f32 v66, v67, v66, s36
	s_cmpk_gt_i32 s46, 0x1ff
	v_fma_f32 v67, -v69, v72, 1.0
	v_fmac_f32_e32 v72, v67, v72
	v_div_scale_f32 v67, vcc, v214, v68, v214
	v_mul_f32_e32 v70, v67, v72
	v_fma_f32 v71, -v69, v70, v67
	v_fmac_f32_e32 v70, v71, v72
	v_fma_f32 v67, -v69, v70, v67
	v_div_fmas_f32 v67, v67, v72, v70
	v_div_fixup_f32 v68, v67, v68, v214
	v_mul_f32_e32 v2, v2, v68
	v_fma_f32 v50, v50, v66, -v2
	v_mul_f32_e32 v2, v3, v68
	v_fma_f32 v51, v51, v66, -v2
	v_mul_f32_e32 v67, v51, v51
	v_mul_f32_e32 v2, v4, v68
	v_fmac_f32_e32 v67, v50, v50
	v_fma_f32 v52, v52, v66, -v2
	v_mul_f32_e32 v2, v5, v68
	v_fmac_f32_e32 v67, v52, v52
	v_fma_f32 v53, v53, v66, -v2
	v_mul_f32_e32 v2, v6, v68
	v_fmac_f32_e32 v67, v53, v53
	v_fma_f32 v54, v54, v66, -v2
	v_mul_f32_e32 v2, v7, v68
	v_fmac_f32_e32 v67, v54, v54
	v_fma_f32 v55, v55, v66, -v2
	v_mul_f32_e32 v2, v8, v68
	v_fmac_f32_e32 v67, v55, v55
	v_fma_f32 v56, v56, v66, -v2
	v_mul_f32_e32 v2, v9, v68
	v_fmac_f32_e32 v67, v56, v56
	v_fma_f32 v57, v57, v66, -v2
	v_mul_f32_e32 v2, v10, v68
	v_fmac_f32_e32 v67, v57, v57
	v_fma_f32 v58, v58, v66, -v2
	v_mul_f32_e32 v2, v11, v68
	v_fmac_f32_e32 v67, v58, v58
	v_fma_f32 v59, v59, v66, -v2
	v_mul_f32_e32 v2, v12, v68
	v_fmac_f32_e32 v67, v59, v59
	v_fma_f32 v60, v60, v66, -v2
	v_mul_f32_e32 v2, v13, v68
	v_fmac_f32_e32 v67, v60, v60
	v_fma_f32 v61, v61, v66, -v2
	v_mul_f32_e32 v14, v14, v68
	v_fmac_f32_e32 v67, v61, v61
	v_fma_f32 v62, v62, v66, -v14
	v_mul_f32_e32 v14, v15, v68
	v_fmac_f32_e32 v67, v62, v62
	v_fma_f32 v63, v63, v66, -v14
	v_mul_f32_e32 v14, v16, v68
	v_lshlrev_b32_e32 v69, 4, v217
	v_fmac_f32_e32 v67, v63, v63
	v_fma_f32 v64, v64, v66, -v14
	v_mul_f32_e32 v14, v17, v68
	global_load_dwordx4 v[2:5], v69, s[12:13] offset:480
	global_load_dwordx4 v[6:9], v69, s[12:13] offset:288
	global_load_dwordx4 v[10:13], v69, s[12:13] offset:256
	v_fmac_f32_e32 v67, v64, v64
	v_fma_f32 v65, v65, v66, -v14
	v_mul_f32_e32 v14, v18, v68
	v_fmac_f32_e32 v67, v65, v65
	v_fma_f32 v70, v34, v66, -v14
	v_mul_f32_e32 v14, v19, v68
	v_fmac_f32_e32 v67, v70, v70
	v_fma_f32 v71, v35, v66, -v14
	v_mul_f32_e32 v14, v20, v68
	v_fmac_f32_e32 v67, v71, v71
	v_fma_f32 v72, v36, v66, -v14
	v_mul_f32_e32 v14, v21, v68
	v_fmac_f32_e32 v67, v72, v72
; DI unsigned pk4_fp8(float a, float b, float c, float d) { int r = 0; r = __builtin_amdgcn_cvt_pk_fp8_f32(a, b, r, false); r = __builtin_amdgcn_cvt_pk_fp8_f32(c, d, r, true); return (unsigned)r; }
; DI float clamp448(float x) { return __builtin_amdgcn_fmed3f(x, -448.0f, 448.0f); }
; DI void attn_unit_d8(unsigned char* lds, const AttnArgs& a) {
;     ...
;     const float r0 = 16.0f / lt0, r1 = 16.0f * a.lam / lt1;
;     float ss = 0.f;
; #pragma unroll
;     for (int d = 0; d < 2; ++d)
; #pragma unroll
;         for (int i = 0; i < 16; ++i) { const float v = o0[d][i] * r0 - o1[d][i] * r1; o0[d][i] = v; ss += v * v; }
;     ss += __shfl_xor(ss, 32);
;     const float rinv = rsqrtf(ss * (1.0f / 64.0f) + EPS) * a.oscale * CAT_SCALE;
;     f32x4 ggv[2][4];
; #pragma unroll
;     for (int d = 0; d < 2; ++d)
; #pragma unroll
;         for (int g = 0; g < 4; ++g) ggv[d][g] = *(const f32x4*)(a.subg + 32 * d + 8 * g + 4 * h);
;     asm volatile("" : "+v"(ggv[0][0]), "+v"(ggv[1][3]));
; #pragma unroll
;     for (int d = 0; d < 2; ++d)
; #pragma unroll
;         for (int g = 0; g < 4; ++g) { const f32x4 gg = ggv[d][g];
;             *(unsigned*)(op + 32 * d + 8 * g) = pk4_fp8(clamp448(o0[d][4 * g] * rinv * gg[0]), clamp448(o0[d][4 * g + 1] * rinv * gg[1]), clamp448(o0[d][4 * g + 2] * rinv * gg[2]), clamp448(o0[d][4 * g + 3] * rinv * gg[3])); }
	v_fma_f32 v73, v37, v66, -v14
	v_mul_f32_e32 v14, v22, v68
	v_fmac_f32_e32 v67, v73, v73
	v_fma_f32 v74, v38, v66, -v14
	v_mul_f32_e32 v14, v23, v68
	v_fmac_f32_e32 v67, v74, v74
	v_fma_f32 v75, v39, v66, -v14
	v_fmac_f32_e32 v67, v75, v75
	v_pk_mul_f32 v[14:15], v[24:25], v[68:69] op_sel_hi:[1,0]
	v_pk_mul_f32 v[22:23], v[32:33], v[68:69] op_sel_hi:[1,0]
	v_pk_fma_f32 v[34:35], v[40:41], v[66:67], v[14:15] op_sel_hi:[1,0,1] neg_lo:[0,0,1] neg_hi:[0,0,1]
	s_nop 0
	v_pk_mul_f32 v[14:15], v[34:35], v[34:35]
	s_nop 0
	v_add_f32_e32 v14, v14, v67
	v_add_f32_e32 v20, v15, v14
	v_pk_mul_f32 v[14:15], v[26:27], v[68:69] op_sel_hi:[1,0]
	s_nop 0
	v_pk_fma_f32 v[36:37], v[42:43], v[66:67], v[14:15] op_sel_hi:[1,0,1] neg_lo:[0,0,1] neg_hi:[0,0,1]
	global_load_dwordx4 v[14:17], v69, s[12:13] offset:320
	v_pk_mul_f32 v[18:19], v[36:37], v[36:37]
	v_pk_fma_f32 v[42:43], v[48:49], v[66:67], v[22:23] op_sel_hi:[1,0,1] neg_lo:[0,0,1] neg_hi:[0,0,1]
	v_add_f32_e32 v18, v18, v20
	v_add_f32_e32 v20, v19, v18
	v_pk_mul_f32 v[18:19], v[28:29], v[68:69] op_sel_hi:[1,0]
	v_pk_mul_f32 v[22:23], v[42:43], v[42:43]
	v_pk_fma_f32 v[38:39], v[44:45], v[66:67], v[18:19] op_sel_hi:[1,0,1] neg_lo:[0,0,1] neg_hi:[0,0,1]
	s_nop 0
	v_pk_mul_f32 v[18:19], v[38:39], v[38:39]
	s_nop 0
	v_add_f32_e32 v18, v18, v20
	v_add_f32_e32 v20, v19, v18
	v_pk_mul_f32 v[18:19], v[30:31], v[68:69] op_sel_hi:[1,0]
	s_nop 0
	v_pk_fma_f32 v[40:41], v[46:47], v[66:67], v[18:19] op_sel_hi:[1,0,1] neg_lo:[0,0,1] neg_hi:[0,0,1]
	s_nop 0
	v_pk_mul_f32 v[18:19], v[40:41], v[40:41]
	s_nop 0
	v_add_f32_e32 v18, v18, v20
	v_add_f32_e32 v24, v19, v18
	v_add_f32_e32 v22, v22, v24
	v_add_f32_e32 v26, v23, v22
	ds_bpermute_b32 v27, v1, v26
	global_load_dwordx4 v[18:21], v69, s[12:13] offset:352
	global_load_dwordx4 v[22:25], v69, s[12:13] offset:448
	s_waitcnt lgkmcnt(0)
	v_add_f32_e32 v26, v26, v27
	v_fmamk_f32 v26, v26, 0x3c800000, v215
	v_mul_f32_e32 v27, 0x4b800000, v26
	v_cmp_gt_f32_e32 vcc, s41, v26
	s_nop 1
	v_cndmask_b32_e32 v30, v26, v27, vcc
	global_load_dwordx4 v[26:29], v69, s[12:13] offset:384
	v_rsq_f32_e32 v32, v30
	v_lshlrev_b64 v[30:31], 10, v[180:181]
	v_lshl_add_u64 v[44:45], s[16:17], 0, v[30:31]
	v_lshl_add_u64 v[44:45], v[44:45], 0, v[178:179]
	v_mul_f32_e32 v30, 0x45800000, v32
	v_cndmask_b32_e32 v30, v32, v30, vcc
	v_mul_f32_e32 v48, v213, v30
	global_load_dwordx4 v[30:33], v69, s[12:13] offset:416
	v_mul_f32_e32 v48, 0x41800000, v48
	s_waitcnt vmcnt(5)
	v_mul_f32_e32 v49, v50, v48
	v_mul_f32_e32 v10, v10, v49
	v_mul_f32_e32 v49, v51, v48
	v_mul_f32_e32 v11, v11, v49
	v_mul_f32_e32 v49, v52, v48
	v_med3_f32 v10, v10, s42, v216
	v_med3_f32 v11, v11, s42, v216
	v_mul_f32_e32 v12, v12, v49
	s_nop 0
	v_cvt_pk_fp8_f32 v49, v10, v11
	v_mul_f32_e32 v10, v53, v48
	v_mul_f32_e32 v10, v13, v10
	v_med3_f32 v12, v12, s42, v216
	v_med3_f32 v10, v10, s42, v216
	v_cvt_pk_fp8_f32 v49, v12, v10 op_sel:[0,0,1]
	v_mul_f32_e32 v10, v54, v48
	v_mul_f32_e32 v6, v6, v10
	v_mul_f32_e32 v10, v55, v48
	v_mul_f32_e32 v7, v7, v10
	v_mul_f32_e32 v10, v56, v48
	v_med3_f32 v6, v6, s42, v216
	v_med3_f32 v7, v7, s42, v216
	v_mul_f32_e32 v8, v8, v10
	s_nop 0
	v_cvt_pk_fp8_f32 v10, v6, v7
	v_mul_f32_e32 v6, v57, v48
	v_mul_f32_e32 v6, v9, v6
	v_med3_f32 v8, v8, s42, v216
	v_med3_f32 v6, v6, s42, v216
	v_cvt_pk_fp8_f32 v10, v8, v6 op_sel:[0,0,1]
	v_add_co_u32_e32 v6, vcc, s43, v44
	v_lshl_add_u64 v[46:47], v[44:45], 0, s[14:15]
	s_nop 0
	v_addc_co_u32_e32 v7, vcc, 0, v45, vcc
	global_store_dword v[6:7], v49, off offset:768
	global_store_dword v[46:47], v10, off offset:8
	v_mul_f32_e32 v6, v58, v48
	v_mul_f32_e32 v7, v59, v48
	s_waitcnt vmcnt(6)
	v_mul_f32_e32 v6, v14, v6
	v_mul_f32_e32 v7, v15, v7
	v_med3_f32 v6, v6, s42, v216
	v_med3_f32 v7, v7, s42, v216
	s_nop 0
	v_cvt_pk_fp8_f32 v9, v6, v7
	v_mul_f32_e32 v8, v60, v48
	v_mul_f32_e32 v6, v61, v48
	v_mul_f32_e32 v8, v16, v8
	v_mul_f32_e32 v6, v17, v6
	v_med3_f32 v8, v8, s42, v216
	v_med3_f32 v6, v6, s42, v216
	v_cvt_pk_fp8_f32 v9, v8, v6 op_sel:[0,0,1]
	v_mul_f32_e32 v6, v62, v48
	v_mul_f32_e32 v7, v63, v48
	s_nop 0
	v_mul_f32_e32 v8, v64, v48
	s_nop 0
	s_waitcnt vmcnt(5)
	v_mul_f32_e32 v6, v18, v6
	v_mul_f32_e32 v7, v19, v7
	v_med3_f32 v6, v6, s42, v216
	v_med3_f32 v7, v7, s42, v216
	v_cvt_pk_fp8_f32 v10, v6, v7
	v_mul_f32_e32 v6, v65, v48
	v_mul_f32_e32 v8, v20, v8
	v_mul_f32_e32 v6, v21, v6
	v_med3_f32 v8, v8, s42, v216
	v_med3_f32 v6, v6, s42, v216
	v_cvt_pk_fp8_f32 v10, v8, v6 op_sel:[0,0,1]
	v_mul_f32_e32 v6, v70, v48
	v_mul_f32_e32 v7, v71, v48
	s_waitcnt vmcnt(3)
	v_mul_f32_e32 v6, v26, v6
	v_mul_f32_e32 v7, v27, v7
	v_med3_f32 v6, v6, s42, v216
	v_med3_f32 v7, v7, s42, v216
	v_cvt_pk_fp8_f32 v11, v6, v7
	v_mul_f32_e32 v8, v72, v48
	v_mul_f32_e32 v6, v73, v48
	v_mul_f32_e32 v8, v28, v8
	v_mul_f32_e32 v6, v29, v6
	v_med3_f32 v8, v8, s42, v216
	v_med3_f32 v6, v6, s42, v216
	v_cvt_pk_fp8_f32 v11, v8, v6 op_sel:[0,0,1]
	v_mul_f32_e32 v6, v74, v48
	v_mul_f32_e32 v7, v75, v48
	s_waitcnt vmcnt(2)
	v_mul_f32_e32 v6, v30, v6
	v_mul_f32_e32 v7, v31, v7
	v_med3_f32 v6, v6, s42, v216
	v_med3_f32 v7, v7, s42, v216
	s_nop 0
	v_cvt_pk_fp8_f32 v12, v6, v7
	v_mul_f32_e32 v8, v34, v48
	v_mul_f32_e32 v6, v35, v48
	v_mul_f32_e32 v8, v32, v8
	v_mul_f32_e32 v6, v33, v6
	v_med3_f32 v8, v8, s42, v216
	v_med3_f32 v6, v6, s42, v216
	v_cvt_pk_fp8_f32 v12, v8, v6 op_sel:[0,0,1]
	v_mul_f32_e32 v6, v36, v48
	v_mul_f32_e32 v7, v37, v48
	v_mul_f32_e32 v6, v22, v6
	v_mul_f32_e32 v7, v23, v7
	global_store_dword v[46:47], v9, off offset:16
	global_store_dword v[46:47], v10, off offset:24
	global_store_dword v[46:47], v11, off offset:32
	global_store_dword v[46:47], v12, off offset:40
	v_med3_f32 v6, v6, s42, v216
	v_med3_f32 v7, v7, s42, v216
	s_nop 0
	v_cvt_pk_fp8_f32 v9, v6, v7
	v_mul_f32_e32 v8, v38, v48
	v_mul_f32_e32 v6, v39, v48
	v_mul_f32_e32 v8, v24, v8
	v_mul_f32_e32 v6, v25, v6
	v_med3_f32 v8, v8, s42, v216
	v_med3_f32 v6, v6, s42, v216
	v_cvt_pk_fp8_f32 v9, v8, v6 op_sel:[0,0,1]
	v_mul_f32_e32 v6, v40, v48
	v_mul_f32_e32 v2, v2, v6
	v_mul_f32_e32 v6, v41, v48
	v_mul_f32_e32 v3, v3, v6
	v_mul_f32_e32 v6, v42, v48
	v_med3_f32 v2, v2, s42, v216
	v_med3_f32 v3, v3, s42, v216
	v_mul_f32_e32 v4, v4, v6
	s_nop 0
	v_cvt_pk_fp8_f32 v6, v2, v3
	v_mul_f32_e32 v2, v43, v48
	v_mul_f32_e32 v2, v5, v2
	v_med3_f32 v4, v4, s42, v216
	v_med3_f32 v2, v2, s42, v216
	v_cvt_pk_fp8_f32 v6, v4, v2 op_sel:[0,0,1]
	global_store_dword v[46:47], v9, off offset:48
	global_store_dword v[46:47], v6, off offset:56
	s_cbranch_scc0 .LBB0_1885
